# speedup vs baseline: 1.0139x; 1.0099x over previous
_Z11k_proj_mfmaPKDF16_PKDv8_DF16_PKfPfPS1_S6_PhS6_PDF16_:
	s_bitcmp1_b32 s2, 3
	s_cbranch_scc0 .Lmy_proj_nosleep
	s_sleep 20
.Lmy_proj_nosleep:
	v_readfirstlane_b32 s21, v0
	s_lshr_b32 s20, s21, 6
	s_and_b32 s24, s2, 3
	s_cmp_lg_u32 s24, 0
	s_cselect_b64 s[8:9], -1, 0
	s_cmp_eq_u32 s24, 2
	s_cselect_b32 s3, 28, 40
	s_cselect_b32 s4, 40, 50
	s_cmp_eq_u32 s24, 1
	s_cselect_b32 s3, 18, s3
	s_cselect_b32 s10, 28, s4
	s_cmp_eq_u32 s24, 0
	s_cselect_b64 s[4:5], -1, 0
	s_load_dwordx2 s[16:17], s[0:1], 0x8
	s_and_b64 s[6:7], s[4:5], exec
	s_cselect_b32 s26, 0, s3
	s_cselect_b32 s3, 18, s10
	s_add_i32 s27, s20, s26
	s_cmp_lt_u32 s27, s3
	s_cselect_b64 s[14:15], -1, 0
	s_cmp_ge_u32 s27, s3
	v_and_b32_e32 v146, 63, v0
	s_cbranch_scc1 .LBB2_2
	s_mul_i32 s6, s27, 0x140
	v_or_b32_e32 v2, s6, v146
	v_mov_b32_e32 v3, 0
	s_waitcnt lgkmcnt(0)
	v_lshl_add_u64 v[4:5], v[2:3], 4, s[16:17]
	s_addk_i32 s6, 0x100
	global_load_dwordx4 v[106:109], v[4:5], off
	global_load_dwordx4 v[114:117], v[4:5], off offset:1024
	global_load_dwordx4 v[126:129], v[4:5], off offset:2048
	global_load_dwordx4 v[134:137], v[4:5], off offset:3072
	v_or_b32_e32 v2, s6, v146
	v_lshl_add_u64 v[2:3], v[2:3], 4, s[16:17]
	global_load_dwordx4 v[138:141], v[2:3], off
